# acquire-invalidate issued at arrival (behind the arrival atomic) at the two barriers that follow balanced phases (FFN-up->down, FFN-down->next layer)
# speedup vs baseline: 1.0314x; 1.0314x over previous
; #define LAS __attribute__((address_space(3)))
; __device__ __forceinline__ int lane_id() { int l; asm volatile("v_mbcnt_lo_u32_b32 %0, -1, 0\n\tv_mbcnt_hi_u32_b32 %0, -1, %0" : "=v"(l)); return l; }
;     __device__ bool next(int i, Unit& u) const {
;         u.hs = -1; long L = (long)i * G + c;
;         if (i == htail) { L = (long)i * G + (c & (G / 2 - 1)); u.hs = c / (G / 2); }
;         if (L >= nwg) return false;
;         int wgid = (int)L; { const int q = nwg / NXCD, r = nwg % NXCD, xcd = wgid % NXCD, off = wgid / NXCD; wgid = (xcd < r ? xcd * (q + 1) : r * (q + 1) + (xcd - r) * q) + off; }
;         const int nig = WGM * nN, gid = wgid / nig, fm = gid * WGM, gsz = (nM - fm) < WGM ? (nM - fm) : WGM;
;         u.pm = fm + ((wgid % nig) % gsz); u.pn = (wgid % nig) / gsz; return true;
; __device__ __forceinline__ Frame make_frame(int wave_s) {
;     Frame F; F.lds = LDS0; { int t_ = wave_s * 64 + lane_id(); asm volatile("" : "+v"(t_)); F.tid = t_; } F.lane = F.tid & 63; F.wave = wave_s;
;     F.G = gridDim.x; { const int bx = blockIdx.x; F.vcu = (F.G % 8 == 0) ? (bx % 8) * (F.G / 8) + bx / 8 : bx; }
;     return F;
; }
; template <class Epi> __device__ __forceinline__ void run_gemm(const pg8::Gemm& g, const Epi& E, int wave_s, bool half_tail = false) {
;     pg8::StaticOrder S; S.init(M, g.N, (int)gridDim.x, (int)blockIdx.x);
;     if (half_tail && S.nwg % S.G == S.G / 2) S.htail = S.nwg / S.G;
;     pg8::gemm_phase<Epi, true, true>(LDS0, (LAS float*)(LDS0 + TAB_OFF), g, S, E, wave_s);
.LBB0_212:
	s_or_b64 exec, exec, s[4:5]
	s_ashr_i32 s75, s74, 31
	s_lshr_b32 s2, s75, 29
	s_add_i32 s2, s74, s2
	s_and_b32 s3, s2, -8
	s_sub_i32 s16, s74, s3
	s_ashr_i32 s14, s2, 3
	s_cmpk_lt_i32 s74, 0x300
	s_cselect_b64 s[2:3], -1, 0
	s_lshr_b32 s0, s0, 8
	v_writelane_b32 v254, s2, 0
	s_lshl_b32 s12, s0, 14
	s_add_i32 s13, s12, 0
	v_writelane_b32 v254, s3, 1
	s_lshr_b32 s2, s16, 31
	s_or_b32 s2, s2, 0x60
	s_mul_i32 s2, s2, s16
	s_add_i32 s3, s2, s14
	s_mul_hi_i32 s4, s3, 0x2aaaaaab
	s_lshr_b32 s5, s4, 31
	s_ashr_i32 s4, s4, 4
	s_add_i32 s4, s4, s5
	s_lshl_b32 s5, s4, 3
	s_mulk_i32 s4, 0x60
	s_sub_i32 s4, s3, s4
	s_lshl_b32 s3, s1, 16
	v_writelane_b32 v254, s3, 2
	s_lshl_b32 s3, s0, 6
	v_writelane_b32 v254, s3, 3
	s_lshl_b32 s3, s1, 1
	s_or_b32 s3, s3, 1
	s_lshl_b32 s8, s3, 3
	s_lshl_b32 s11, s3, 14
	s_lshl_b32 s0, s1, 11
	s_lshl_b32 s3, s3, 10
	s_add_i32 s15, s13, s0
	v_writelane_b32 v254, s13, 4
	s_add_i32 s17, s3, s13
	s_add_i32 s13, 0, 0x2000
	s_add_i32 s12, s12, s13
	s_add_i32 s18, s12, s0
	s_add_i32 s3, s3, s12
	v_writelane_b32 v254, s15, 5
	s_add_i32 s12, s15, 0x8000
	v_writelane_b32 v254, s12, 6
	v_writelane_b32 v254, s17, 7
	s_add_i32 s12, s17, 0x8000
	v_writelane_b32 v254, s12, 8
	v_writelane_b32 v254, s18, 9
	s_add_i32 s12, s18, 0x8000
	v_writelane_b32 v254, s12, 10
	v_writelane_b32 v254, s3, 11
	s_add_i32 s3, s3, 0x8000
	v_writelane_b32 v254, s3, 12
	s_lshl_b32 s3, s1, 5
	v_writelane_b32 v254, s3, 13
	s_lshl_b32 s3, s78, 2
	s_add_i32 s3, s3, 0
	s_add_i32 s3, s3, 0x20000
	v_writelane_b32 v254, s3, 14
	s_lshl_b32 s3, s78, 12
	s_sub_i32 s6, 64, s5
	s_lshl_b32 s7, s1, 4
	s_lshl_b32 s9, s1, 15
	s_add_i32 s3, s3, 0
	s_min_u32 s6, s6, 8
	s_and_b32 s9, s9, 0x8000
	s_and_b32 s10, s7, 32
	s_and_b32 s11, s11, 0xc000
	v_writelane_b32 v254, s3, 15
	s_add_i32 s3, s3, 0x18000
	s_cmpk_lt_i32 s74, 0x100
	v_writelane_b32 v254, s3, 16
	s_cselect_b64 s[18:19], -1, 0
	s_lshl_b32 s3, s16, 6
	s_sub_i32 s2, s2, s3
	s_add_i32 s2, s2, s14
	s_ashr_i32 s3, s2, 31
	s_lshr_b32 s3, s3, 27
	s_add_i32 s3, s2, s3
	v_writelane_b32 v254, s18, 17
	s_ashr_i32 s12, s3, 5
	s_lshl_b32 s12, s12, 3
	v_writelane_b32 v254, s19, 18
	v_writelane_b32 v254, s14, 19
	s_sub_i32 s14, 64, s12
	s_andn2_b32 s3, s3, 31
	s_min_u32 s14, s14, 8
	s_sub_i32 s15, s2, s3
	s_cmpk_lt_i32 s74, 0x1c0
	s_mul_i32 s3, s16, 24
	s_cselect_b64 s[18:19], -1, 0
	s_add_i32 s2, s2, s3
	v_writelane_b32 v254, s18, 20
	s_mul_hi_i32 s3, s2, 0x92492493
	s_add_i32 s3, s3, s2
	v_writelane_b32 v254, s19, 21
	v_writelane_b32 v254, s16, 22
	s_lshr_b32 s16, s3, 31
	s_ashr_i32 s3, s3, 5
	s_add_i32 s3, s3, s16
	s_lshl_b32 s16, s3, 3
	s_mul_i32 s3, s3, 56
	s_lshl_b32 s19, s78, 3
	s_sub_i32 s18, s2, s3
	s_and_b32 s2, s19, 0x1fffffe0
	v_writelane_b32 v254, s2, 23
	s_lshl_b32 s1, s1, 6
	v_writelane_b32 v254, s1, 24
	s_lshl_b32 s1, s78, 8
	s_add_i32 s1, s1, 0
	s_add_i32 s1, s1, 0x14000
	v_writelane_b32 v254, s1, 25
	s_lshl_b32 s1, s78, 10
	s_add_i32 s2, s1, 0
	v_writelane_b32 v254, s2, 26
	s_add_i32 s3, s2, 0x6000
	v_writelane_b32 v254, s3, 27
	s_add_i32 s2, s2, 0x8000
	v_writelane_b32 v254, s2, 28
	s_sext_i32_i8 s2, s4
	s_waitcnt vmcnt(15)
	v_cvt_f32_ubyte0_e32 v1, s6
	s_waitcnt lgkmcnt(0)
	v_cvt_f32_i32_e32 v0, s2
	v_rcp_iflag_f32_e32 v2, v1
	s_add_i32 s1, s1, s13
	s_sub_i32 s17, 64, s16
	v_writelane_b32 v254, s1, 29
	v_mul_f32_e32 v2, v0, v2
	v_trunc_f32_e32 v2, v2
	v_fma_f32 v0, -v2, v1, v0
	v_cvt_i32_f32_e32 v2, v2
	s_ashr_i32 s1, s2, 30
	s_min_u32 s17, s17, 8
	s_or_b32 s1, s1, 1
	v_cmp_ge_f32_e64 s[2:3], |v0|, v1
	s_and_b64 s[2:3], s[2:3], exec
	s_cselect_b32 s1, s1, 0
	v_readfirstlane_b32 s2, v2
	s_add_i32 s2, s2, s1
	s_sext_i32_i8 s1, s2
	v_writelane_b32 v254, s1, 30
	s_mul_i32 s1, s2, s6
	s_sub_i32 s1, s4, s1
	s_sext_i32_i8 s1, s1
	s_add_i32 s20, s5, s1
	s_sext_i32_i8 s1, s15
	v_cvt_f32_ubyte0_e32 v1, s14
	v_cvt_f32_i32_e32 v0, s1
	v_rcp_iflag_f32_e32 v2, v1
	s_mov_b32 s4, s20
	s_ashr_i32 s21, s20, 31
	v_writelane_b32 v254, s4, 31
	v_mul_f32_e32 v2, v0, v2
	s_bfe_i64 s[2:3], s[2:3], 0x80000
	v_writelane_b32 v254, s5, 32
	s_lshl_b64 s[4:5], s[20:21], 18
	v_writelane_b32 v254, s4, 33
	v_trunc_f32_e32 v2, v2
	s_lshl_b64 s[2:3], s[2:3], 18
	v_writelane_b32 v254, s5, 34
	v_fma_f32 v0, -v2, v1, v0
	v_cvt_i32_f32_e32 v2, v2
	v_writelane_b32 v254, s2, 35
	s_ashr_i32 s1, s1, 30
	s_or_b32 s1, s1, 1
	v_writelane_b32 v254, s3, 36
	v_cmp_ge_f32_e64 s[2:3], |v0|, v1
	s_and_b64 s[2:3], s[2:3], exec
	s_cselect_b32 s1, s1, 0
	v_readfirstlane_b32 s2, v2
	s_add_i32 s1, s2, s1
	s_mul_i32 s2, s1, s14
	s_sub_i32 s2, s15, s2
	s_sext_i32_i8 s2, s2
	s_add_i32 s2, s12, s2
	v_writelane_b32 v254, s2, 37
	s_sext_i32_i8 s2, s18
	v_cvt_f32_ubyte0_e32 v1, s17
	v_cvt_f32_i32_e32 v0, s2
	v_rcp_iflag_f32_e32 v2, v1
	s_sext_i32_i8 s1, s1
	v_writelane_b32 v254, s1, 38
	s_ashr_i32 s1, s2, 30
	v_mul_f32_e32 v2, v0, v2
	v_trunc_f32_e32 v2, v2
	v_fma_f32 v0, -v2, v1, v0
	v_cvt_i32_f32_e32 v2, v2
	s_or_b32 s1, s1, 1
	v_cmp_ge_f32_e64 s[2:3], |v0|, v1
	s_and_b64 s[2:3], s[2:3], exec
	s_cselect_b32 s1, s1, 0
	v_readfirstlane_b32 s2, v2
	s_add_i32 s1, s2, s1
	s_sext_i32_i8 s2, s1
	s_mul_i32 s1, s1, s17
	s_sub_i32 s1, s18, s1
	s_sext_i32_i8 s1, s1
	v_writelane_b32 v254, s2, 39
	s_add_i32 s1, s16, s1
	v_writelane_b32 v254, s1, 40
	s_abs_i32 s1, s74
	v_writelane_b32 v254, s1, 41
	s_add_i32 s1, 0, 0x20960
	v_writelane_b32 v254, s1, 42
	s_add_i32 s1, 0, 0x20964
	v_writelane_b32 v254, s1, 43
	s_lshl_b32 s1, s7, 1
	v_writelane_b32 v254, s1, 44
	s_lshl_b32 s1, s8, 1
	v_writelane_b32 v254, s1, 45
	s_lshl_b32 s1, s9, 1
	v_writelane_b32 v254, s1, 46
	s_lshl_b32 s1, s10, 1
	v_writelane_b32 v254, s1, 47
	s_lshl_b32 s1, s11, 1
	v_writelane_b32 v254, s1, 48
	s_add_i32 s1, 0, 0x20010
	v_writelane_b32 v254, s1, 49
	s_add_i32 s1, 0, 0x19400
	v_writelane_b32 v254, s1, 50
	s_lshl_b32 s1, s19, 1
	v_writelane_b32 v254, s1, 51
	s_lshl_b32 s0, s0, 1
	v_writelane_b32 v254, s0, 52
	s_add_i32 s0, 0, 0x200
	v_writelane_b32 v254, s0, 53
	s_add_i32 s0, 0, 0xc200
	v_writelane_b32 v254, s0, 54
	s_mov_b32 s1, 0
	v_writelane_b32 v254, s0, 55
	v_mov_b32_e32 v1, 0
	s_mov_b32 s95, 0x20000
	v_writelane_b32 v254, s1, 56
	v_writelane_b32 v254, s74, 57
	s_mov_b32 s67, 0x42fe0000
	s_mov_b32 s68, 0x40c0c00
	v_writelane_b32 v254, s75, 58
	v_writelane_b32 v254, s76, 59
	v_mov_b32_e32 v228, 0x358637bd
	s_mov_b32 s84, 0x800000
	v_writelane_b32 v254, s77, 60
	v_writelane_b32 v254, s78, 61
	v_writelane_b32 v254, s79, 62
	v_writelane_b32 v254, s80, 63
	s_movk_i32 s86, 0xff
	s_movk_i32 s87, 0xc0
	v_writelane_b32 v255, s81, 0
	v_writelane_b32 v255, s82, 1
	v_mov_b32_e32 v229, 1
	s_brev_b32 s94, -2
	v_bfrev_b32_e32 v230, 1
	v_mov_b32_e32 v231, 0xff800000
	v_mov_b64_e32 v[202:203], 0x100
	v_mov_b64_e32 v[204:205], 0xff
	v_mov_b32_e32 v240, v1
	v_mov_b32_e32 v241, v1
	v_mov_b32_e32 v242, v1
	v_mov_b32_e32 v243, v1
	v_mov_b32_e32 v232, 0x9f
	v_mov_b32_e32 v233, 0x446
	s_movk_i32 s88, 0x3a8
	s_movk_i32 s89, 0xff60
	s_movk_i32 s92, 0xfc58
	s_brev_b32 s85, 1
	s_movk_i32 s93, 0xf00
	s_mov_b32 s54, 0
	s_mov_b64 s[90:91], 0x80
	v_writelane_b32 v255, s83, 2
	s_barrier
	s_branch .LBB0_216
; __device__ __forceinline__ unsigned xb_ld(unsigned* p)              { return __hip_atomic_load(p, __ATOMIC_RELAXED, __HIP_MEMORY_SCOPE_AGENT); }
; #define XB_SPIN(cond, bar) do { unsigned _sp = 0; while (cond) { __builtin_amdgcn_s_sleep(1); \
;     if ((++_sp & 255u) == 0u) { if (xb_ld(&(bar)[XB_TMO])) break; if (_sp > XB_SPIN_CAP) { atomicAdd(&(bar)[XB_TMO], 1u); break; } } } } while (0)
; __device__ __forceinline__ void xcd_barrier_impl(const XcdBarrier& b, bool leader) {
;     ...
;             if (og + 1u != (tg + 1u) * nx) XB_SPIN(xb_ld(&bar[XB_TOP]) < (tg + 1u) * nx, bar);
;             __builtin_amdgcn_fence(__ATOMIC_ACQUIRE, "agent");
;             asm volatile("s_waitcnt vmcnt(0)" ::: "memory");
;         } else {
;             XB_SPIN(xb_ld(&bar[XB_TOP]) < (gen + 1u) * nx, bar);
;             __builtin_amdgcn_fence(__ATOMIC_ACQUIRE, "agent");
;             asm volatile("s_waitcnt vmcnt(0)" ::: "memory");
.LBB0_213:
	s_or_b64 exec, exec, s[10:11]
	s_waitcnt vmcnt(0)
	s_waitcnt vmcnt(0)

; __device__ __forceinline__ unsigned xb_ld(unsigned* p)              { return __hip_atomic_load(p, __ATOMIC_RELAXED, __HIP_MEMORY_SCOPE_AGENT); }
; __device__ __forceinline__ unsigned xb_add(unsigned* p, unsigned v) { return __hip_atomic_fetch_add(p, v, __ATOMIC_RELAXED, __HIP_MEMORY_SCOPE_AGENT); }
; #define XB_SPIN(cond, bar) do { unsigned _sp = 0; while (cond) { __builtin_amdgcn_s_sleep(1); \
;     if ((++_sp & 255u) == 0u) { if (xb_ld(&(bar)[XB_TMO])) break; if (_sp > XB_SPIN_CAP) { atomicAdd(&(bar)[XB_TMO], 1u); break; } } } } while (0)
; __device__ __forceinline__ void xcd_barrier_impl(const XcdBarrier& b, bool leader) {
;     ...
;         const unsigned old = xb_add(&bar[XB_XSUB(b.x)], 1u);
;         const unsigned gen = old / nloc;
;         if (old + 1u == (gen + 1u) * nloc) {
;             __builtin_amdgcn_fence(__ATOMIC_RELEASE, "agent");
;             asm volatile("s_waitcnt vmcnt(0)" ::: "memory");
;             const unsigned og = xb_add(&bar[XB_TOP], 1u);
;             const unsigned tg = og / nx;
;             if (og + 1u != (tg + 1u) * nx) XB_SPIN(xb_ld(&bar[XB_TOP]) < (tg + 1u) * nx, bar);
.LBB0_2132:
	s_or_b64 exec, exec, s[10:11]
	buffer_inv sc1
	v_cvt_f32_u32_e32 v5, v2
	s_waitcnt vmcnt(1)
	v_readfirstlane_b32 s0, v4
	v_sub_u32_e32 v4, 0, v2
	v_rcp_iflag_f32_e32 v5, v5
	v_add_u32_e32 v3, s0, v3
	v_mul_f32_e32 v5, 0x4f7ffffe, v5
	v_cvt_u32_f32_e32 v5, v5
	v_mul_lo_u32 v4, v4, v5
	v_mul_hi_u32 v4, v5, v4
	v_add_u32_e32 v4, v5, v4
	v_mul_hi_u32 v4, v3, v4
	v_mul_lo_u32 v5, v4, v2
	v_sub_u32_e32 v5, v3, v5
	v_add_u32_e32 v6, 1, v4
	v_cmp_ge_u32_e32 vcc, v5, v2
	s_nop 1
	v_cndmask_b32_e32 v4, v4, v6, vcc
	v_sub_u32_e32 v6, v5, v2
	v_cndmask_b32_e32 v5, v5, v6, vcc
	v_add_u32_e32 v6, 1, v4
	v_cmp_ge_u32_e32 vcc, v5, v2
	v_add_u32_e32 v5, 1, v3
	s_nop 0
	v_cndmask_b32_e32 v4, v4, v6, vcc
	v_add_u32_e32 v3, 1, v4
	v_mul_lo_u32 v2, v3, v2
	v_cmp_ne_u32_e32 vcc, v5, v2
	s_and_saveexec_b64 s[0:1], vcc
	s_xor_b64 s[10:11], exec, s[0:1]
	s_cbranch_execz .LBB0_2146
	v_mov_b32_e32 v2, 0x7000
	global_load_dword v2, v2, s[8:9] offset:1024 sc1
	s_add_u32 s12, s8, 0x7400
	s_waitcnt lgkmcnt(0)
	v_mul_lo_u32 v0, v3, v0
	s_addc_u32 s13, s9, 0
	s_waitcnt vmcnt(0)
	v_cmp_lt_u32_e32 vcc, v2, v0
	s_and_saveexec_b64 s[14:15], vcc
	s_cbranch_execz .LBB0_2145
	s_add_u32 s16, s8, 0x4200
	s_addc_u32 s17, s9, 0
	s_mov_b32 s0, 1
	s_mov_b64 s[18:19], 0
	s_branch .LBB0_2136

; __device__ __forceinline__ unsigned xb_ld(unsigned* p)              { return __hip_atomic_load(p, __ATOMIC_RELAXED, __HIP_MEMORY_SCOPE_AGENT); }
; #define XB_SPIN(cond, bar) do { unsigned _sp = 0; while (cond) { __builtin_amdgcn_s_sleep(1); \
;     if ((++_sp & 255u) == 0u) { if (xb_ld(&(bar)[XB_TMO])) break; if (_sp > XB_SPIN_CAP) { atomicAdd(&(bar)[XB_TMO], 1u); break; } } } } while (0)
; __device__ __forceinline__ float* karg_out() { return (float*)(GAS float*)karg_u64<14>(); }
; __device__ __forceinline__ unsigned char* karg_ws() { return (unsigned char*)(GAS unsigned char*)karg_u64<15>(); }
; __device__ __forceinline__ void xcd_barrier_impl(const XcdBarrier& b, bool leader) {
;     ...
;             __builtin_amdgcn_fence(__ATOMIC_ACQUIRE, "agent");
;             asm volatile("s_waitcnt vmcnt(0)" ::: "memory");
;         } else {
;             XB_SPIN(xb_ld(&bar[XB_TOP]) < (gen + 1u) * nx, bar);
;             __builtin_amdgcn_fence(__ATOMIC_ACQUIRE, "agent");
;             asm volatile("s_waitcnt vmcnt(0)" ::: "memory");
;         }
;     }
;     __syncthreads();
; __global__ void __launch_bounds__(512, 2) trunk_fwd(Args args) {
;     ...
;         { unsigned char* ws = karg_ws(); float* OUT = karg_out();
;           pg8::Gemm g{(const bf16_t*)(ws + WS_H2), (const bf16_t*)(ws + WS_W_DN + layer * SZ_DN), D, FF, FF, nullptr};
;           pg8::EpiRes E{(const float*)nullptr, (layer + 1 == DEPTH) ? OUT : (float*)nullptr, ws, false};
.LBB0_2162:
	s_or_b64 exec, exec, s[12:13]
	s_waitcnt vmcnt(0)
	s_waitcnt vmcnt(0)
.LBB0_2163:
	s_or_b64 exec, exec, s[6:7]
	s_waitcnt lgkmcnt(0)
	s_barrier
	s_load_dwordx2 s[8:9], s[76:77], 0x78
	s_waitcnt lgkmcnt(0)
	s_load_dwordx2 s[6:7], s[76:77], 0x70
	s_waitcnt lgkmcnt(0)
	v_readlane_b32 s2, v254, 17
	v_mbcnt_lo_u32_b32 v0, -1, 0
	v_mbcnt_hi_u32_b32 v0, -1, v0
	v_readlane_b32 s3, v254, 18
	s_waitcnt vmcnt(12)
	v_add_u32_e32 v18, s79, v0
	s_and_b64 vcc, exec, s[2:3]
	v_readfirstlane_b32 s0, v18
	s_cbranch_vccz .LBB0_2165
	v_readlane_b32 s1, v254, 37
	v_readlane_b32 s2, v254, 38
	s_mov_b32 s12, s1

; __device__ __forceinline__ unsigned xb_ld(unsigned* p)              { return __hip_atomic_load(p, __ATOMIC_RELAXED, __HIP_MEMORY_SCOPE_AGENT); }
; __device__ __forceinline__ unsigned xb_add(unsigned* p, unsigned v) { return __hip_atomic_fetch_add(p, v, __ATOMIC_RELAXED, __HIP_MEMORY_SCOPE_AGENT); }
; #define XB_SPIN(cond, bar) do { unsigned _sp = 0; while (cond) { __builtin_amdgcn_s_sleep(1); \
;     if ((++_sp & 255u) == 0u) { if (xb_ld(&(bar)[XB_TMO])) break; if (_sp > XB_SPIN_CAP) { atomicAdd(&(bar)[XB_TMO], 1u); break; } } } } while (0)
; __device__ __forceinline__ void xcd_barrier_impl(const XcdBarrier& b, bool leader) {
;     ...
;         const unsigned old = xb_add(&bar[XB_XSUB(b.x)], 1u);
;         const unsigned gen = old / nloc;
;         if (old + 1u == (gen + 1u) * nloc) {
;             __builtin_amdgcn_fence(__ATOMIC_RELEASE, "agent");
;             asm volatile("s_waitcnt vmcnt(0)" ::: "memory");
;             const unsigned og = xb_add(&bar[XB_TOP], 1u);
;             const unsigned tg = og / nx;
;             if (og + 1u != (tg + 1u) * nx) XB_SPIN(xb_ld(&bar[XB_TOP]) < (tg + 1u) * nx, bar);
.LBB0_2302:
	s_or_b64 exec, exec, s[8:9]
	buffer_inv sc1
	v_cvt_f32_u32_e32 v5, v2
	s_waitcnt vmcnt(1)
	v_readfirstlane_b32 s0, v4
	v_sub_u32_e32 v4, 0, v2
	v_rcp_iflag_f32_e32 v5, v5
	v_add_u32_e32 v3, s0, v3
	v_mul_f32_e32 v5, 0x4f7ffffe, v5
	v_cvt_u32_f32_e32 v5, v5
	v_mul_lo_u32 v4, v4, v5
	v_mul_hi_u32 v4, v5, v4
	v_add_u32_e32 v4, v5, v4
	v_mul_hi_u32 v4, v3, v4
	v_mul_lo_u32 v5, v4, v2
	v_sub_u32_e32 v5, v3, v5
	v_add_u32_e32 v6, 1, v4
	v_cmp_ge_u32_e32 vcc, v5, v2
	s_nop 1
	v_cndmask_b32_e32 v4, v4, v6, vcc
	v_sub_u32_e32 v6, v5, v2
	v_cndmask_b32_e32 v5, v5, v6, vcc
	v_add_u32_e32 v6, 1, v4
	v_cmp_ge_u32_e32 vcc, v5, v2
	v_add_u32_e32 v5, 1, v3
	s_nop 0
	v_cndmask_b32_e32 v4, v4, v6, vcc
	v_add_u32_e32 v3, 1, v4
	v_mul_lo_u32 v2, v3, v2
	v_cmp_ne_u32_e32 vcc, v5, v2
	s_and_saveexec_b64 s[0:1], vcc
	s_xor_b64 s[8:9], exec, s[0:1]
	s_cbranch_execz .LBB0_2316
	v_mov_b32_e32 v2, 0x7000
	global_load_dword v2, v2, s[6:7] offset:1024 sc1
	s_add_u32 s10, s6, 0x7400
	s_waitcnt lgkmcnt(0)
	v_mul_lo_u32 v0, v3, v0
	s_addc_u32 s11, s7, 0
	s_waitcnt vmcnt(0)
	v_cmp_lt_u32_e32 vcc, v2, v0
	s_and_saveexec_b64 s[12:13], vcc
	s_cbranch_execz .LBB0_2315
	s_add_u32 s16, s6, 0x4200
	s_addc_u32 s17, s7, 0
	s_mov_b32 s0, 1
	s_mov_b64 s[18:19], 0
	s_branch .LBB0_2306

; __device__ __forceinline__ unsigned xb_ld(unsigned* p)              { return __hip_atomic_load(p, __ATOMIC_RELAXED, __HIP_MEMORY_SCOPE_AGENT); }
; #define XB_SPIN(cond, bar) do { unsigned _sp = 0; while (cond) { __builtin_amdgcn_s_sleep(1); \
;     if ((++_sp & 255u) == 0u) { if (xb_ld(&(bar)[XB_TMO])) break; if (_sp > XB_SPIN_CAP) { atomicAdd(&(bar)[XB_TMO], 1u); break; } } } } while (0)
; __device__ __forceinline__ void xcd_barrier_impl(const XcdBarrier& b, bool leader) {
;     ...
;             if (og + 1u != (tg + 1u) * nx) XB_SPIN(xb_ld(&bar[XB_TOP]) < (tg + 1u) * nx, bar);
;             __builtin_amdgcn_fence(__ATOMIC_ACQUIRE, "agent");
;             asm volatile("s_waitcnt vmcnt(0)" ::: "memory");
;         } else {
;             XB_SPIN(xb_ld(&bar[XB_TOP]) < (gen + 1u) * nx, bar);
;             __builtin_amdgcn_fence(__ATOMIC_ACQUIRE, "agent");
;             asm volatile("s_waitcnt vmcnt(0)" ::: "memory");
.LBB0_2312:
	s_or_b64 exec, exec, s[18:19]
	s_xor_b64 s[0:1], s[20:21], -1
	s_and_saveexec_b64 s[2:3], s[0:1]
	s_xor_b64 s[2:3], exec, s[2:3]
	s_cbranch_execz .LBB0_2315
	s_mov_b64 s[10:11], exec
	v_mbcnt_lo_u32_b32 v0, s10, 0
	v_mbcnt_hi_u32_b32 v0, s11, v0
	v_cmp_eq_u32_e32 vcc, 0, v0
	s_and_b64 s[0:1], exec, vcc
	s_mov_b64 exec, s[0:1]
	s_cbranch_execz .LBB0_2315
	s_bcnt1_i32_b64 s0, s[10:11]
	v_mov_b32_e32 v0, s0
	global_atomic_add v1, v0, s[16:17]
.LBB0_2315:
	s_or_b64 exec, exec, s[12:13]
	s_waitcnt vmcnt(0)
	s_waitcnt vmcnt(0)
.LBB0_2316:
	s_andn2_saveexec_b64 s[0:1], s[8:9]
	s_cbranch_execnz .LBB0_2317
	s_getpc_b64 s[98:99]
